# diff attention: MFMA-result pad before the row-max trimmed from 32 to 22 wait states (20 required)
# speedup vs baseline: 1.0007x; 1.0007x over previous
; #define SBAR() __builtin_amdgcn_sched_barrier(0)
; __device__ __forceinline__ void mask_tile_perm(f32x16& p0, f32x16& p1, int dq) {
;     const float NEG = -__builtin_inff();
; #pragma unroll
;     for (int r = 0; r < 16; ++r) { const int c = 16 * (r & 3) + (r >> 2);
;         if (dq - c < 0) p0[r] = NEG;
;         if (dq - c - 4 < 0) p1[r] = NEG; }
; }
; template <int KB, bool LOWREG = false>
; __device__ __forceinline__ void qkt_f8(f32x16& p0, f32x16& p1, const char* K_lds, int r32, int hi, const i32x8 (&q8)[2]) {
;     ...
;     if constexpr (LOWREG) {
;     ...
;         i32x8 f0 = KF8(0, 0), f1 = KF8(0, 1);
;         SBAR();
;         asm volatile("v_mfma_f32_32x32x64_f8f6f4 %0, %1, %2, 0" : "=&v"(p0) : "v"(f0), "v"(q8[0]));
;         asm volatile("v_mfma_f32_32x32x64_f8f6f4 %0, %1, %2, 0" : "=&v"(p1) : "v"(f1), "v"(q8[0]));
;         SBAR();
;         f0 = KF8(1, 0); f1 = KF8(1, 1);
;         SBAR();
;         asm volatile("v_mfma_f32_32x32x64_f8f6f4 %0, %1, %2, %0" : "+v"(p0) : "v"(f0), "v"(q8[1]));
;         asm volatile("v_mfma_f32_32x32x64_f8f6f4 %0, %1, %2, %0" : "+v"(p1) : "v"(f1), "v"(q8[1]));
;         asm volatile("s_nop 15\n\ts_nop 15" ::: "memory");
;         SBAR();
.LBB0_1213:
	s_setprio 1
	v_mov_b32_e32 v2, v213
	v_mov_b32_e32 v4, v202
	s_add_i32 s76, 0, 0x10000
	s_cmp_lg_u32 s76, -1
	v_lshrrev_b32_e32 v12, 1, v4
	s_cselect_b32 s6, s76, 0
	v_lshlrev_b32_e32 v2, 1, v2
	v_bfe_u32 v5, v4, 1, 3
	v_lshl_add_u32 v13, v4, 7, s6
	v_bitop3_b32 v4, v12, v2, 7 bitop3:0x6c
	v_lshl_add_u32 v8, v4, 4, v13
	v_bitop3_b32 v4, v2, v5, 1 bitop3:0x36
	v_lshl_add_u32 v14, v4, 4, v13
	ds_read_b128 v[4:7], v8
	ds_read_b128 v[242:245], v8 offset:4096
	ds_read_b128 v[8:11], v14
	ds_read_b128 v[246:249], v14 offset:4096
	s_waitcnt lgkmcnt(0)
	v_mfma_f32_32x32x64_f8f6f4 v[162:177], v[4:11], v[178:185], 0
	v_mfma_f32_32x32x64_f8f6f4 v[146:161], v[242:249], v[178:185], 0
	v_add_u32_e32 v4, 4, v2
	v_bitop3_b32 v4, v4, v12, 7 bitop3:0x78
	v_add_u32_e32 v2, 5, v2
	v_lshl_add_u32 v8, v4, 4, v13
	v_bitop3_b32 v2, v2, v12, 7 bitop3:0x78
	v_lshl_add_u32 v2, v2, 4, v13
	ds_read_b128 v[4:7], v8
	ds_read_b128 v[242:245], v8 offset:4096
	ds_read_b128 v[8:11], v2
	ds_read_b128 v[246:249], v2 offset:4096
	s_waitcnt lgkmcnt(0)
	v_mfma_f32_32x32x64_f8f6f4 v[162:177], v[4:11], v[186:193], v[162:177]
	v_mfma_f32_32x32x64_f8f6f4 v[146:161], v[242:249], v[186:193], v[146:161]
	s_nop 15
	s_nop 5
	s_cmp_le_i32 s78, s80
	s_cbranch_scc1 .LBB0_1215
	v_cmp_gt_i32_e64 s[58:59], 50, v240
	v_cmp_gt_i32_e64 s[66:67], 51, v240
	v_cmp_gt_i32_e64 s[50:51], 49, v240
	s_and_b64 s[58:59], s[66:67], s[58:59]
	v_cmp_gt_i32_e64 s[42:43], 48, v240
	s_and_b64 s[50:51], s[58:59], s[50:51]
	v_cmp_gt_i32_e64 s[40:41], 32, v240
	s_and_b64 s[42:43], s[50:51], s[42:43]
	v_cmp_gt_i32_e64 s[38:39], 16, v240
	s_and_b64 s[40:41], s[42:43], s[40:41]
	v_cmp_gt_i32_e64 s[36:37], 0, v240
	s_and_b64 s[38:39], s[40:41], s[38:39]
	s_and_b64 s[36:37], s[38:39], s[36:37]
	v_cmp_gt_i32_e64 s[28:29], 54, v240
	v_cndmask_b32_e64 v162, v162, v210, s[36:37]
	v_cmp_gt_i32_e64 s[36:37], 55, v240
	v_cmp_gt_i32_e64 s[20:21], 53, v240
	s_and_b64 s[28:29], s[36:37], s[28:29]
	v_cmp_gt_i32_e64 s[12:13], 52, v240
	s_and_b64 s[20:21], s[28:29], s[20:21]
	v_cmp_gt_i32_e64 s[8:9], 36, v240
	v_cmp_gt_i32_e64 s[48:49], 33, v240
	v_cmp_gt_i32_e64 s[16:17], 37, v240
	v_cmp_gt_i32_e64 s[56:57], 34, v240
	v_cmp_gt_i32_e64 s[24:25], 38, v240
	v_cmp_gt_i32_e64 s[64:65], 35, v240
	v_cmp_gt_i32_e64 s[34:35], 39, v240
	s_and_b64 s[12:13], s[20:21], s[12:13]
	v_cmp_gt_i32_e64 s[6:7], 20, v240
	v_cmp_gt_i32_e64 s[46:47], 17, v240
	v_cmp_gt_i32_e64 s[14:15], 21, v240
	v_cmp_gt_i32_e64 s[54:55], 18, v240
	v_cmp_gt_i32_e64 s[22:23], 22, v240
	v_cmp_gt_i32_e64 s[62:63], 19, v240
	v_cmp_gt_i32_e64 s[30:31], 23, v240
	s_and_b64 s[64:65], s[66:67], s[64:65]
	s_and_b64 s[56:57], s[58:59], s[56:57]
	s_and_b64 s[48:49], s[50:51], s[48:49]
	s_and_b64 s[34:35], s[36:37], s[34:35]
	s_and_b64 s[24:25], s[28:29], s[24:25]
	s_and_b64 s[16:17], s[20:21], s[16:17]
	s_and_b64 s[8:9], s[12:13], s[8:9]
	v_cmp_gt_i32_e32 vcc, 4, v240
	v_cmp_gt_i32_e64 s[44:45], 1, v240
	v_cmp_gt_i32_e64 s[10:11], 5, v240
	v_cmp_gt_i32_e64 s[52:53], 2, v240
	v_cmp_gt_i32_e64 s[18:19], 6, v240
	v_cmp_gt_i32_e64 s[60:61], 3, v240
	v_cmp_gt_i32_e64 s[26:27], 7, v240
	s_and_b64 s[62:63], s[64:65], s[62:63]
	s_and_b64 s[54:55], s[56:57], s[54:55]
	s_and_b64 s[46:47], s[48:49], s[46:47]
	s_and_b64 s[30:31], s[34:35], s[30:31]
	s_and_b64 s[22:23], s[24:25], s[22:23]
	s_and_b64 s[14:15], s[16:17], s[14:15]
	s_and_b64 s[6:7], s[8:9], s[6:7]
	v_cndmask_b32_e64 v173, v173, v210, s[58:59]
	v_cndmask_b32_e64 v169, v169, v210, s[50:51]
	s_and_b64 s[58:59], s[62:63], s[60:61]
	v_cndmask_b32_e64 v165, v165, v210, s[42:43]
	s_and_b64 s[50:51], s[54:55], s[52:53]
	s_and_b64 s[42:43], s[46:47], s[44:45]
	s_and_b64 s[26:27], s[30:31], s[26:27]
	s_and_b64 s[18:19], s[22:23], s[18:19]
	s_and_b64 s[10:11], s[14:15], s[10:11]
	s_and_b64 vcc, s[6:7], vcc
	v_cndmask_b32_e64 v177, v177, v210, s[66:67]
	v_cndmask_b32_e64 v176, v176, v210, s[64:65]
	v_cndmask_b32_e64 v175, v175, v210, s[62:63]
	v_cndmask_b32_e64 v172, v172, v210, s[56:57]
	v_cndmask_b32_e64 v174, v174, v210, s[58:59]
	v_cndmask_b32_e64 v171, v171, v210, s[54:55]
	v_cndmask_b32_e64 v168, v168, v210, s[48:49]
	v_cndmask_b32_e64 v170, v170, v210, s[50:51]
	v_cndmask_b32_e64 v167, v167, v210, s[46:47]
	v_cndmask_b32_e64 v164, v164, v210, s[40:41]
	v_cndmask_b32_e64 v166, v166, v210, s[42:43]
	v_cndmask_b32_e64 v163, v163, v210, s[38:39]
	v_cndmask_b32_e64 v161, v161, v210, s[36:37]
	v_cndmask_b32_e64 v160, v160, v210, s[34:35]
	v_cndmask_b32_e64 v157, v157, v210, s[28:29]
	v_cndmask_b32_e64 v159, v159, v210, s[30:31]
	v_cndmask_b32_e64 v156, v156, v210, s[24:25]
	v_cndmask_b32_e64 v153, v153, v210, s[20:21]
	v_cndmask_b32_e64 v158, v158, v210, s[26:27]
	v_cndmask_b32_e64 v155, v155, v210, s[22:23]
	v_cndmask_b32_e64 v152, v152, v210, s[16:17]
	v_cndmask_b32_e64 v149, v149, v210, s[12:13]
	v_cndmask_b32_e64 v154, v154, v210, s[18:19]
	v_cndmask_b32_e64 v151, v151, v210, s[14:15]
	v_cndmask_b32_e64 v148, v148, v210, s[8:9]
	v_cndmask_b32_e64 v150, v150, v210, s[10:11]
	v_cndmask_b32_e64 v147, v147, v210, s[6:7]
	v_cndmask_b32_e32 v146, v146, v210, vcc

; #define SBAR() __builtin_amdgcn_sched_barrier(0)
; __device__ __forceinline__ void mask_tile_perm(f32x16& p0, f32x16& p1, int dq) {
;     const float NEG = -__builtin_inff();
; #pragma unroll
;     for (int r = 0; r < 16; ++r) { const int c = 16 * (r & 3) + (r >> 2);
;         if (dq - c < 0) p0[r] = NEG;
;         if (dq - c - 4 < 0) p1[r] = NEG; }
; }
; template <int KB, bool LOWREG = false>
; __device__ __forceinline__ void qkt_f8(f32x16& p0, f32x16& p1, const char* K_lds, int r32, int hi, const i32x8 (&q8)[2]) {
;     ...
;     if constexpr (LOWREG) {
;     ...
;         i32x8 f0 = KF8(0, 0), f1 = KF8(0, 1);
;         SBAR();
;         asm volatile("v_mfma_f32_32x32x64_f8f6f4 %0, %1, %2, 0" : "=&v"(p0) : "v"(f0), "v"(q8[0]));
;         asm volatile("v_mfma_f32_32x32x64_f8f6f4 %0, %1, %2, 0" : "=&v"(p1) : "v"(f1), "v"(q8[0]));
;         SBAR();
;         f0 = KF8(1, 0); f1 = KF8(1, 1);
;         SBAR();
;         asm volatile("v_mfma_f32_32x32x64_f8f6f4 %0, %1, %2, %0" : "+v"(p0) : "v"(f0), "v"(q8[1]));
;         asm volatile("v_mfma_f32_32x32x64_f8f6f4 %0, %1, %2, %0" : "+v"(p1) : "v"(f1), "v"(q8[1]));
;         asm volatile("s_nop 15\n\ts_nop 15" ::: "memory");
;         SBAR();
.LBB0_1231:
	s_setprio 1
	s_cmp_lg_u32 s76, -1
	v_mov_b32_e32 v4, v213
	v_mov_b32_e32 v5, v202
	s_cselect_b32 s6, s76, 0
	s_addk_i32 s6, 0x4000
	v_lshrrev_b32_e32 v12, 1, v5
	v_lshlrev_b32_e32 v14, 1, v4
	v_bfe_u32 v6, v5, 1, 3
	v_lshl_add_u32 v13, v5, 7, s6
	v_bitop3_b32 v4, v12, v14, 7 bitop3:0x6c
	v_lshl_add_u32 v8, v4, 4, v13
	v_bitop3_b32 v4, v14, v6, 1 bitop3:0x36
	v_lshl_add_u32 v15, v4, 4, v13
	ds_read_b128 v[4:7], v8
	ds_read_b128 v[244:247], v8 offset:4096
	ds_read_b128 v[8:11], v15
	ds_read_b128 v[248:251], v15 offset:4096
	s_waitcnt lgkmcnt(0)
	v_mfma_f32_32x32x64_f8f6f4 v[162:177], v[4:11], v[178:185], 0
	v_mfma_f32_32x32x64_f8f6f4 v[146:161], v[244:251], v[178:185], 0
	v_add_u32_e32 v4, 4, v14
	v_bitop3_b32 v4, v4, v12, 7 bitop3:0x78
	v_lshl_add_u32 v8, v4, 4, v13
	v_add_u32_e32 v4, 5, v14
	v_bitop3_b32 v4, v4, v12, 7 bitop3:0x78
	v_lshl_add_u32 v12, v4, 4, v13
	ds_read_b128 v[4:7], v8
	ds_read_b128 v[244:247], v8 offset:4096
	ds_read_b128 v[8:11], v12
	ds_read_b128 v[248:251], v12 offset:4096
	s_waitcnt lgkmcnt(0)
	v_mfma_f32_32x32x64_f8f6f4 v[162:177], v[4:11], v[186:193], v[162:177]
	v_mfma_f32_32x32x64_f8f6f4 v[146:161], v[244:251], v[186:193], v[146:161]
	s_nop 15
	s_nop 5
	s_add_i32 s6, s78, 64
	s_cmp_le_i32 s6, s80
	s_cbranch_scc1 .LBB0_1233
	v_subrev_u32_e32 v4, 64, v240
	v_cmp_gt_i32_e64 s[58:59], 50, v4
	v_cmp_gt_i32_e64 s[66:67], 51, v4
	v_cmp_gt_i32_e64 s[50:51], 49, v4
	s_and_b64 s[58:59], s[66:67], s[58:59]
	v_cmp_gt_i32_e64 s[42:43], 48, v4
	s_and_b64 s[50:51], s[58:59], s[50:51]
	v_cmp_gt_i32_e64 s[40:41], 32, v4
	s_and_b64 s[42:43], s[50:51], s[42:43]
	v_cmp_gt_i32_e64 s[38:39], 16, v4
	s_and_b64 s[40:41], s[42:43], s[40:41]
	v_cmp_gt_i32_e64 s[36:37], 0, v4
	s_and_b64 s[38:39], s[40:41], s[38:39]
	s_and_b64 s[36:37], s[38:39], s[36:37]
	v_cmp_gt_i32_e64 s[28:29], 54, v4
	v_cndmask_b32_e64 v162, v162, v210, s[36:37]
	v_cmp_gt_i32_e64 s[36:37], 55, v4
	v_cmp_gt_i32_e64 s[20:21], 53, v4
	s_and_b64 s[28:29], s[36:37], s[28:29]
	v_cmp_gt_i32_e64 s[12:13], 52, v4
	s_and_b64 s[20:21], s[28:29], s[20:21]
	v_cmp_gt_i32_e64 s[8:9], 36, v4
	v_cmp_gt_i32_e64 s[48:49], 33, v4
	v_cmp_gt_i32_e64 s[16:17], 37, v4
	v_cmp_gt_i32_e64 s[56:57], 34, v4
	v_cmp_gt_i32_e64 s[24:25], 38, v4
	v_cmp_gt_i32_e64 s[64:65], 35, v4
	v_cmp_gt_i32_e64 s[34:35], 39, v4
	s_and_b64 s[12:13], s[20:21], s[12:13]
	v_cmp_gt_i32_e64 s[6:7], 20, v4
	v_cmp_gt_i32_e64 s[46:47], 17, v4
	v_cmp_gt_i32_e64 s[14:15], 21, v4
	v_cmp_gt_i32_e64 s[54:55], 18, v4
	v_cmp_gt_i32_e64 s[22:23], 22, v4
	v_cmp_gt_i32_e64 s[62:63], 19, v4
	v_cmp_gt_i32_e64 s[30:31], 23, v4
	s_and_b64 s[64:65], s[66:67], s[64:65]
	s_and_b64 s[56:57], s[58:59], s[56:57]
	s_and_b64 s[48:49], s[50:51], s[48:49]
	s_and_b64 s[34:35], s[36:37], s[34:35]
	s_and_b64 s[24:25], s[28:29], s[24:25]
	s_and_b64 s[16:17], s[20:21], s[16:17]
	s_and_b64 s[8:9], s[12:13], s[8:9]
	v_cmp_gt_i32_e32 vcc, 4, v4
	v_cmp_gt_i32_e64 s[44:45], 1, v4
	v_cmp_gt_i32_e64 s[10:11], 5, v4
	v_cmp_gt_i32_e64 s[52:53], 2, v4
	v_cmp_gt_i32_e64 s[18:19], 6, v4
	v_cmp_gt_i32_e64 s[60:61], 3, v4
	v_cmp_gt_i32_e64 s[26:27], 7, v4
	s_and_b64 s[62:63], s[64:65], s[62:63]
	s_and_b64 s[54:55], s[56:57], s[54:55]
	s_and_b64 s[46:47], s[48:49], s[46:47]
	s_and_b64 s[30:31], s[34:35], s[30:31]
	s_and_b64 s[22:23], s[24:25], s[22:23]
	s_and_b64 s[14:15], s[16:17], s[14:15]
	s_and_b64 s[6:7], s[8:9], s[6:7]
	v_cndmask_b32_e64 v173, v173, v210, s[58:59]
	v_cndmask_b32_e64 v169, v169, v210, s[50:51]
	s_and_b64 s[58:59], s[62:63], s[60:61]
	v_cndmask_b32_e64 v165, v165, v210, s[42:43]
	s_and_b64 s[50:51], s[54:55], s[52:53]
	s_and_b64 s[42:43], s[46:47], s[44:45]
	s_and_b64 s[26:27], s[30:31], s[26:27]
	s_and_b64 s[18:19], s[22:23], s[18:19]
	s_and_b64 s[10:11], s[14:15], s[10:11]
	s_and_b64 vcc, s[6:7], vcc
	v_cndmask_b32_e64 v177, v177, v210, s[66:67]
	v_cndmask_b32_e64 v176, v176, v210, s[64:65]
	v_cndmask_b32_e64 v175, v175, v210, s[62:63]
	v_cndmask_b32_e64 v172, v172, v210, s[56:57]
	v_cndmask_b32_e64 v174, v174, v210, s[58:59]
	v_cndmask_b32_e64 v171, v171, v210, s[54:55]
	v_cndmask_b32_e64 v168, v168, v210, s[48:49]
	v_cndmask_b32_e64 v170, v170, v210, s[50:51]
	v_cndmask_b32_e64 v167, v167, v210, s[46:47]
	v_cndmask_b32_e64 v164, v164, v210, s[40:41]
	v_cndmask_b32_e64 v166, v166, v210, s[42:43]
	v_cndmask_b32_e64 v163, v163, v210, s[38:39]
	v_cndmask_b32_e64 v161, v161, v210, s[36:37]
	v_cndmask_b32_e64 v160, v160, v210, s[34:35]
	v_cndmask_b32_e64 v157, v157, v210, s[28:29]
	v_cndmask_b32_e64 v159, v159, v210, s[30:31]
	v_cndmask_b32_e64 v156, v156, v210, s[24:25]
	v_cndmask_b32_e64 v153, v153, v210, s[20:21]
	v_cndmask_b32_e64 v158, v158, v210, s[26:27]
	v_cndmask_b32_e64 v155, v155, v210, s[22:23]
	v_cndmask_b32_e64 v152, v152, v210, s[16:17]
	v_cndmask_b32_e64 v149, v149, v210, s[12:13]
	v_cndmask_b32_e64 v154, v154, v210, s[18:19]
	v_cndmask_b32_e64 v151, v151, v210, s[14:15]
	v_cndmask_b32_e64 v148, v148, v210, s[8:9]
	v_cndmask_b32_e64 v150, v150, v210, s[10:11]
	v_cndmask_b32_e64 v147, v147, v210, s[6:7]
	v_cndmask_b32_e32 v146, v146, v210, vcc

; #define SBAR() __builtin_amdgcn_sched_barrier(0)
; __device__ __forceinline__ void mask_tile_perm(f32x16& p0, f32x16& p1, int dq) {
;     const float NEG = -__builtin_inff();
; #pragma unroll
;     for (int r = 0; r < 16; ++r) { const int c = 16 * (r & 3) + (r >> 2);
;         if (dq - c < 0) p0[r] = NEG;
;         if (dq - c - 4 < 0) p1[r] = NEG; }
; }
; template <int KB, bool LOWREG = false>
; __device__ __forceinline__ void qkt_f8(f32x16& p0, f32x16& p1, const char* K_lds, int r32, int hi, const i32x8 (&q8)[2]) {
;     ...
;     if constexpr (LOWREG) {
;     ...
;         i32x8 f0 = KF8(0, 0), f1 = KF8(0, 1);
;         SBAR();
;         asm volatile("v_mfma_f32_32x32x64_f8f6f4 %0, %1, %2, 0" : "=&v"(p0) : "v"(f0), "v"(q8[0]));
;         asm volatile("v_mfma_f32_32x32x64_f8f6f4 %0, %1, %2, 0" : "=&v"(p1) : "v"(f1), "v"(q8[0]));
;         SBAR();
;         f0 = KF8(1, 0); f1 = KF8(1, 1);
;         SBAR();
;         asm volatile("v_mfma_f32_32x32x64_f8f6f4 %0, %1, %2, %0" : "+v"(p0) : "v"(f0), "v"(q8[1]));
;         asm volatile("v_mfma_f32_32x32x64_f8f6f4 %0, %1, %2, %0" : "+v"(p1) : "v"(f1), "v"(q8[1]));
;         asm volatile("s_nop 15\n\ts_nop 15" ::: "memory");
;         SBAR();
.LBB0_1253:
	s_setprio 1
	s_add_i32 s76, 0, 0x10000
	v_mov_b32_e32 v2, v202
	v_mov_b32_e32 v4, v213
	s_cmp_lg_u32 s76, -1
	s_cselect_b32 s6, s76, 0
	v_lshrrev_b32_e32 v12, 1, v2
	v_lshlrev_b32_e32 v13, 1, v4
	v_bfe_u32 v5, v2, 1, 3
	v_lshl_add_u32 v2, v2, 7, s6
	v_bitop3_b32 v4, v12, v13, 7 bitop3:0x6c
	v_lshl_add_u32 v8, v4, 4, v2
	v_bitop3_b32 v4, v13, v5, 1 bitop3:0x36
	v_lshl_add_u32 v14, v4, 4, v2
	ds_read_b128 v[4:7], v8
	ds_read_b128 v[224:227], v8 offset:4096
	ds_read_b128 v[8:11], v14
	ds_read_b128 v[228:231], v14 offset:4096
	s_waitcnt lgkmcnt(0)
	v_mfma_f32_32x32x64_f8f6f4 v[162:177], v[4:11], v[178:185], 0
	v_mfma_f32_32x32x64_f8f6f4 v[146:161], v[224:231], v[178:185], 0
	v_add_u32_e32 v4, 4, v13
	v_bitop3_b32 v4, v4, v12, 7 bitop3:0x78
	v_lshl_add_u32 v8, v4, 4, v2
	v_add_u32_e32 v4, 5, v13
	v_bitop3_b32 v4, v4, v12, 7 bitop3:0x78
	v_lshl_add_u32 v2, v4, 4, v2
	ds_read_b128 v[4:7], v8
	ds_read_b128 v[224:227], v8 offset:4096
	ds_read_b128 v[8:11], v2
	ds_read_b128 v[228:231], v2 offset:4096
	s_waitcnt lgkmcnt(0)
	v_mfma_f32_32x32x64_f8f6f4 v[162:177], v[4:11], v[186:193], v[162:177]
	v_mfma_f32_32x32x64_f8f6f4 v[146:161], v[224:231], v[186:193], v[146:161]
	s_nop 15
	s_nop 5
	s_cmp_le_i32 s88, s80
	s_cbranch_scc1 .LBB0_1255
	v_cmp_gt_i32_e64 s[58:59], 50, v201
	v_cmp_gt_i32_e64 s[66:67], 51, v201
	v_cmp_gt_i32_e64 s[50:51], 49, v201
	s_and_b64 s[58:59], s[66:67], s[58:59]
	v_cmp_gt_i32_e64 s[42:43], 48, v201
	s_and_b64 s[50:51], s[58:59], s[50:51]
	v_cmp_gt_i32_e64 s[40:41], 32, v201
	s_and_b64 s[42:43], s[50:51], s[42:43]
	v_cmp_gt_i32_e64 s[38:39], 16, v201
	s_and_b64 s[40:41], s[42:43], s[40:41]
	v_cmp_gt_i32_e64 s[36:37], 0, v201
	s_and_b64 s[38:39], s[40:41], s[38:39]
	s_and_b64 s[36:37], s[38:39], s[36:37]
	v_cmp_gt_i32_e64 s[28:29], 54, v201
	v_cndmask_b32_e64 v162, v162, v210, s[36:37]
	v_cmp_gt_i32_e64 s[36:37], 55, v201
	v_cmp_gt_i32_e64 s[20:21], 53, v201
	s_and_b64 s[28:29], s[36:37], s[28:29]
	v_cmp_gt_i32_e64 s[12:13], 52, v201
	s_and_b64 s[20:21], s[28:29], s[20:21]
	v_cmp_gt_i32_e64 s[8:9], 36, v201
	v_cmp_gt_i32_e64 s[48:49], 33, v201
	v_cmp_gt_i32_e64 s[16:17], 37, v201
	v_cmp_gt_i32_e64 s[56:57], 34, v201
	v_cmp_gt_i32_e64 s[24:25], 38, v201
	v_cmp_gt_i32_e64 s[64:65], 35, v201
	v_cmp_gt_i32_e64 s[34:35], 39, v201
	s_and_b64 s[12:13], s[20:21], s[12:13]
	v_cmp_gt_i32_e64 s[6:7], 20, v201
	v_cmp_gt_i32_e64 s[46:47], 17, v201
	v_cmp_gt_i32_e64 s[14:15], 21, v201
	v_cmp_gt_i32_e64 s[54:55], 18, v201
	v_cmp_gt_i32_e64 s[22:23], 22, v201
	v_cmp_gt_i32_e64 s[62:63], 19, v201
	v_cmp_gt_i32_e64 s[30:31], 23, v201
	s_and_b64 s[64:65], s[66:67], s[64:65]
	s_and_b64 s[56:57], s[58:59], s[56:57]
	s_and_b64 s[48:49], s[50:51], s[48:49]
	s_and_b64 s[34:35], s[36:37], s[34:35]
	s_and_b64 s[24:25], s[28:29], s[24:25]
	s_and_b64 s[16:17], s[20:21], s[16:17]
	s_and_b64 s[8:9], s[12:13], s[8:9]
	v_cmp_gt_i32_e32 vcc, 4, v201
	v_cmp_gt_i32_e64 s[44:45], 1, v201
	v_cmp_gt_i32_e64 s[10:11], 5, v201
	v_cmp_gt_i32_e64 s[52:53], 2, v201
	v_cmp_gt_i32_e64 s[18:19], 6, v201
	v_cmp_gt_i32_e64 s[60:61], 3, v201
	v_cmp_gt_i32_e64 s[26:27], 7, v201
	s_and_b64 s[62:63], s[64:65], s[62:63]
	s_and_b64 s[54:55], s[56:57], s[54:55]
	s_and_b64 s[46:47], s[48:49], s[46:47]
	s_and_b64 s[30:31], s[34:35], s[30:31]
	s_and_b64 s[22:23], s[24:25], s[22:23]
	s_and_b64 s[14:15], s[16:17], s[14:15]
	s_and_b64 s[6:7], s[8:9], s[6:7]
	v_cndmask_b32_e64 v173, v173, v210, s[58:59]
	v_cndmask_b32_e64 v169, v169, v210, s[50:51]
	s_and_b64 s[58:59], s[62:63], s[60:61]
	v_cndmask_b32_e64 v165, v165, v210, s[42:43]
	s_and_b64 s[50:51], s[54:55], s[52:53]
	s_and_b64 s[42:43], s[46:47], s[44:45]
	s_and_b64 s[26:27], s[30:31], s[26:27]
	s_and_b64 s[18:19], s[22:23], s[18:19]
	s_and_b64 s[10:11], s[14:15], s[10:11]
	s_and_b64 vcc, s[6:7], vcc
	v_cndmask_b32_e64 v177, v177, v210, s[66:67]
	v_cndmask_b32_e64 v176, v176, v210, s[64:65]
	v_cndmask_b32_e64 v175, v175, v210, s[62:63]
	v_cndmask_b32_e64 v172, v172, v210, s[56:57]
	v_cndmask_b32_e64 v174, v174, v210, s[58:59]
	v_cndmask_b32_e64 v171, v171, v210, s[54:55]
	v_cndmask_b32_e64 v168, v168, v210, s[48:49]
	v_cndmask_b32_e64 v170, v170, v210, s[50:51]
	v_cndmask_b32_e64 v167, v167, v210, s[46:47]
	v_cndmask_b32_e64 v164, v164, v210, s[40:41]
	v_cndmask_b32_e64 v166, v166, v210, s[42:43]
	v_cndmask_b32_e64 v163, v163, v210, s[38:39]
	v_cndmask_b32_e64 v161, v161, v210, s[36:37]
	v_cndmask_b32_e64 v160, v160, v210, s[34:35]
	v_cndmask_b32_e64 v157, v157, v210, s[28:29]
	v_cndmask_b32_e64 v159, v159, v210, s[30:31]
	v_cndmask_b32_e64 v156, v156, v210, s[24:25]
	v_cndmask_b32_e64 v153, v153, v210, s[20:21]
	v_cndmask_b32_e64 v158, v158, v210, s[26:27]
	v_cndmask_b32_e64 v155, v155, v210, s[22:23]
	v_cndmask_b32_e64 v152, v152, v210, s[16:17]
	v_cndmask_b32_e64 v149, v149, v210, s[12:13]
	v_cndmask_b32_e64 v154, v154, v210, s[18:19]
	v_cndmask_b32_e64 v151, v151, v210, s[14:15]
	v_cndmask_b32_e64 v148, v148, v210, s[8:9]
	v_cndmask_b32_e64 v150, v150, v210, s[10:11]
	v_cndmask_b32_e64 v147, v147, v210, s[6:7]
	v_cndmask_b32_e32 v146, v146, v210, vcc

; #define SBAR() __builtin_amdgcn_sched_barrier(0)
; __device__ __forceinline__ void mask_tile_perm(f32x16& p0, f32x16& p1, int dq) {
;     const float NEG = -__builtin_inff();
; #pragma unroll
;     for (int r = 0; r < 16; ++r) { const int c = 16 * (r & 3) + (r >> 2);
;         if (dq - c < 0) p0[r] = NEG;
;         if (dq - c - 4 < 0) p1[r] = NEG; }
; }
; template <int KB, bool LOWREG = false>
; __device__ __forceinline__ void qkt_f8(f32x16& p0, f32x16& p1, const char* K_lds, int r32, int hi, const i32x8 (&q8)[2]) {
;     ...
;     if constexpr (LOWREG) {
;     ...
;         i32x8 f0 = KF8(0, 0), f1 = KF8(0, 1);
;         SBAR();
;         asm volatile("v_mfma_f32_32x32x64_f8f6f4 %0, %1, %2, 0" : "=&v"(p0) : "v"(f0), "v"(q8[0]));
;         asm volatile("v_mfma_f32_32x32x64_f8f6f4 %0, %1, %2, 0" : "=&v"(p1) : "v"(f1), "v"(q8[0]));
;         SBAR();
;         f0 = KF8(1, 0); f1 = KF8(1, 1);
;         SBAR();
;         asm volatile("v_mfma_f32_32x32x64_f8f6f4 %0, %1, %2, %0" : "+v"(p0) : "v"(f0), "v"(q8[1]));
;         asm volatile("v_mfma_f32_32x32x64_f8f6f4 %0, %1, %2, %0" : "+v"(p1) : "v"(f1), "v"(q8[1]));
;         asm volatile("s_nop 15\n\ts_nop 15" ::: "memory");
;         SBAR();
.LBB0_1271:
	s_setprio 1
	s_cmp_lg_u32 s76, -1
	v_mov_b32_e32 v4, v202
	v_mov_b32_e32 v5, v213
	s_cselect_b32 s6, s76, 0
	s_addk_i32 s6, 0x4000
	v_lshrrev_b32_e32 v12, 1, v4
	v_lshlrev_b32_e32 v14, 1, v5
	v_bfe_u32 v6, v4, 1, 3
	v_lshl_add_u32 v13, v4, 7, s6
	v_bitop3_b32 v4, v12, v14, 7 bitop3:0x6c
	v_lshl_add_u32 v8, v4, 4, v13
	v_bitop3_b32 v4, v14, v6, 1 bitop3:0x36
	v_lshl_add_u32 v15, v4, 4, v13
	ds_read_b128 v[4:7], v8
	ds_read_b128 v[224:227], v8 offset:4096
	ds_read_b128 v[8:11], v15
	ds_read_b128 v[228:231], v15 offset:4096
	s_waitcnt lgkmcnt(0)
	v_mfma_f32_32x32x64_f8f6f4 v[162:177], v[4:11], v[178:185], 0
	v_mfma_f32_32x32x64_f8f6f4 v[146:161], v[224:231], v[178:185], 0
	v_add_u32_e32 v4, 4, v14
	v_bitop3_b32 v4, v4, v12, 7 bitop3:0x78
	v_lshl_add_u32 v8, v4, 4, v13
	v_add_u32_e32 v4, 5, v14
	v_bitop3_b32 v4, v4, v12, 7 bitop3:0x78
	v_lshl_add_u32 v12, v4, 4, v13
	ds_read_b128 v[4:7], v8
	ds_read_b128 v[224:227], v8 offset:4096
	ds_read_b128 v[8:11], v12
	ds_read_b128 v[228:231], v12 offset:4096
	s_waitcnt lgkmcnt(0)
	v_mfma_f32_32x32x64_f8f6f4 v[162:177], v[4:11], v[186:193], v[162:177]
	v_mfma_f32_32x32x64_f8f6f4 v[146:161], v[224:231], v[186:193], v[146:161]
	s_nop 15
	s_nop 5
	s_add_i32 s6, s88, 64
	s_cmp_le_i32 s6, s80
	s_cbranch_scc1 .LBB0_1273
	v_subrev_u32_e32 v4, 64, v201
	v_cmp_gt_i32_e64 s[58:59], 50, v4
	v_cmp_gt_i32_e64 s[66:67], 51, v4
	v_cmp_gt_i32_e64 s[50:51], 49, v4
	s_and_b64 s[58:59], s[66:67], s[58:59]
	v_cmp_gt_i32_e64 s[42:43], 48, v4
	s_and_b64 s[50:51], s[58:59], s[50:51]
	v_cmp_gt_i32_e64 s[40:41], 32, v4
	s_and_b64 s[42:43], s[50:51], s[42:43]
	v_cmp_gt_i32_e64 s[38:39], 16, v4
	s_and_b64 s[40:41], s[42:43], s[40:41]
	v_cmp_gt_i32_e64 s[36:37], 0, v4
	s_and_b64 s[38:39], s[40:41], s[38:39]
	s_and_b64 s[36:37], s[38:39], s[36:37]
	v_cmp_gt_i32_e64 s[28:29], 54, v4
	v_cndmask_b32_e64 v162, v162, v210, s[36:37]
	v_cmp_gt_i32_e64 s[36:37], 55, v4
	v_cmp_gt_i32_e64 s[20:21], 53, v4
	s_and_b64 s[28:29], s[36:37], s[28:29]
	v_cmp_gt_i32_e64 s[12:13], 52, v4
	s_and_b64 s[20:21], s[28:29], s[20:21]
	v_cmp_gt_i32_e64 s[8:9], 36, v4
	v_cmp_gt_i32_e64 s[48:49], 33, v4
	v_cmp_gt_i32_e64 s[16:17], 37, v4
	v_cmp_gt_i32_e64 s[56:57], 34, v4
	v_cmp_gt_i32_e64 s[24:25], 38, v4
	v_cmp_gt_i32_e64 s[64:65], 35, v4
	v_cmp_gt_i32_e64 s[34:35], 39, v4
	s_and_b64 s[12:13], s[20:21], s[12:13]
	v_cmp_gt_i32_e64 s[6:7], 20, v4
	v_cmp_gt_i32_e64 s[46:47], 17, v4
	v_cmp_gt_i32_e64 s[14:15], 21, v4
	v_cmp_gt_i32_e64 s[54:55], 18, v4
	v_cmp_gt_i32_e64 s[22:23], 22, v4
	v_cmp_gt_i32_e64 s[62:63], 19, v4
	v_cmp_gt_i32_e64 s[30:31], 23, v4
	s_and_b64 s[64:65], s[66:67], s[64:65]
	s_and_b64 s[56:57], s[58:59], s[56:57]
	s_and_b64 s[48:49], s[50:51], s[48:49]
	s_and_b64 s[34:35], s[36:37], s[34:35]
	s_and_b64 s[24:25], s[28:29], s[24:25]
	s_and_b64 s[16:17], s[20:21], s[16:17]
	s_and_b64 s[8:9], s[12:13], s[8:9]
	v_cmp_gt_i32_e32 vcc, 4, v4
	v_cmp_gt_i32_e64 s[44:45], 1, v4
	v_cmp_gt_i32_e64 s[10:11], 5, v4
	v_cmp_gt_i32_e64 s[52:53], 2, v4
	v_cmp_gt_i32_e64 s[18:19], 6, v4
	v_cmp_gt_i32_e64 s[60:61], 3, v4
	v_cmp_gt_i32_e64 s[26:27], 7, v4
	s_and_b64 s[62:63], s[64:65], s[62:63]
	s_and_b64 s[54:55], s[56:57], s[54:55]
	s_and_b64 s[46:47], s[48:49], s[46:47]
	s_and_b64 s[30:31], s[34:35], s[30:31]
	s_and_b64 s[22:23], s[24:25], s[22:23]
	s_and_b64 s[14:15], s[16:17], s[14:15]
	s_and_b64 s[6:7], s[8:9], s[6:7]
	v_cndmask_b32_e64 v173, v173, v210, s[58:59]
	v_cndmask_b32_e64 v169, v169, v210, s[50:51]
	s_and_b64 s[58:59], s[62:63], s[60:61]
	v_cndmask_b32_e64 v165, v165, v210, s[42:43]
	s_and_b64 s[50:51], s[54:55], s[52:53]
	s_and_b64 s[42:43], s[46:47], s[44:45]
	s_and_b64 s[26:27], s[30:31], s[26:27]
	s_and_b64 s[18:19], s[22:23], s[18:19]
	s_and_b64 s[10:11], s[14:15], s[10:11]
	s_and_b64 vcc, s[6:7], vcc
	v_cndmask_b32_e64 v177, v177, v210, s[66:67]
	v_cndmask_b32_e64 v176, v176, v210, s[64:65]
	v_cndmask_b32_e64 v175, v175, v210, s[62:63]
	v_cndmask_b32_e64 v172, v172, v210, s[56:57]
	v_cndmask_b32_e64 v174, v174, v210, s[58:59]
	v_cndmask_b32_e64 v171, v171, v210, s[54:55]
	v_cndmask_b32_e64 v168, v168, v210, s[48:49]
	v_cndmask_b32_e64 v170, v170, v210, s[50:51]
	v_cndmask_b32_e64 v167, v167, v210, s[46:47]
	v_cndmask_b32_e64 v164, v164, v210, s[40:41]
	v_cndmask_b32_e64 v166, v166, v210, s[42:43]
	v_cndmask_b32_e64 v163, v163, v210, s[38:39]
	v_cndmask_b32_e64 v161, v161, v210, s[36:37]
	v_cndmask_b32_e64 v160, v160, v210, s[34:35]
	v_cndmask_b32_e64 v157, v157, v210, s[28:29]
	v_cndmask_b32_e64 v159, v159, v210, s[30:31]
	v_cndmask_b32_e64 v156, v156, v210, s[24:25]
	v_cndmask_b32_e64 v153, v153, v210, s[20:21]
	v_cndmask_b32_e64 v158, v158, v210, s[26:27]
	v_cndmask_b32_e64 v155, v155, v210, s[22:23]
	v_cndmask_b32_e64 v152, v152, v210, s[16:17]
	v_cndmask_b32_e64 v149, v149, v210, s[12:13]
	v_cndmask_b32_e64 v154, v154, v210, s[18:19]
	v_cndmask_b32_e64 v151, v151, v210, s[14:15]
	v_cndmask_b32_e64 v148, v148, v210, s[8:9]
	v_cndmask_b32_e64 v150, v150, v210, s[10:11]
	v_cndmask_b32_e64 v147, v147, v210, s[6:7]
	v_cndmask_b32_e32 v146, v146, v210, vcc
